# speedup vs baseline: 1.0317x; 1.0317x over previous
_Z7k_gemm1ILi0EEvPKDF16_S1_PDF16_PK15HIP_vector_typeIiLj2EEPKfS8_S2_PKt:
	s_mov_b32 s100, s2
	s_load_dwordx4 s[12:15], s[0:1], 0x18
	s_load_dwordx2 s[24:25], s[0:1], 0x28
	s_mul_i32 s4, s2, 20
	s_ashr_i32 s5, s4, 31
	s_lshl_b64 s[4:5], s[4:5], 3
	s_waitcnt lgkmcnt(0)
	s_add_u32 s20, s12, s4
	s_addc_u32 s21, s13, s5
	s_load_dwordx8 s[4:11], s[20:21], 0x0
	s_load_dwordx4 s[16:19], s[20:21], 0x20
	s_load_dwordx2 s[12:13], s[20:21], 0x30
	v_readfirstlane_b32 s56, v0
	s_mov_b32 s29, 0
	s_waitcnt lgkmcnt(0)
	s_cmp_lt_i32 s4, 0
	s_cselect_b64 s[20:21], -1, 0
	s_and_b64 vcc, exec, s[20:21]
	s_cbranch_vccnz .LBB4_2
	s_lshl_b32 s3, s5, 8
	s_and_b32 s28, s3, 0xff00
	s_bfe_u32 s3, s5, 0x80008
	s_lshl_b32 s83, s3, 1
	s_lshl_b32 s3, s4, 11
	s_and_b32 s82, s4, 0xff
	s_bfe_u32 s81, s4, 0x80010
	s_and_b32 s30, s3, 0x7f80000
	s_mov_b32 s31, s29
	s_branch .LBB4_3

.LBB4_18:
.LBB4_24:
	s_and_b64 s[50:51], s[42:43], exec
	s_cselect_b32 s52, s39, s47
	s_cselect_b32 s53, s38, s46
	s_cselect_b32 s54, s41, s45
	s_cselect_b32 s55, s40, s44
	s_add_u32 s28, s46, 0x100
	s_addc_u32 s84, s47, 0
	s_and_b64 s[50:51], s[48:49], exec
	s_cselect_b32 s51, s52, s84
	s_cselect_b32 s50, s53, s28
	s_add_u32 s28, s44, 0x100
	s_addc_u32 s84, s45, 0
	s_and_b64 s[48:49], s[48:49], exec
	s_cselect_b32 s49, s54, s84
	s_cselect_b32 s48, s55, s28
	s_mov_b32 m0, s59
	v_add_u32_e32 v229, s76, v234
	v_lshl_add_u64 v[130:131], s[48:49], 0, v[216:217]
	ds_read_b128 v[74:77], v229
	ds_read_b128 v[86:89], v229 offset:1024
	ds_read_b128 v[98:101], v229 offset:2048
	ds_read_b128 v[106:109], v229 offset:3072
	global_load_lds_dwordx4 v[130:131], off
	v_lshl_add_u64 v[132:133], s[48:49], 0, v[218:219]
	s_mov_b32 m0, s60
	s_nop 0
	global_load_lds_dwordx4 v[132:133], off
	s_barrier
	s_waitcnt lgkmcnt(0)
	s_setprio 1
	s_waitcnt lgkmcnt(0)
	v_mfma_f32_16x16x32_f16 v[94:97], v[74:77], v[46:49], 0
	v_mfma_f32_16x16x32_f16 v[46:49], v[98:101], v[46:49], 0
	v_mfma_f32_16x16x32_f16 v[94:97], v[86:89], v[50:53], v[94:97]
	v_mfma_f32_16x16x32_f16 v[50:53], v[106:109], v[50:53], v[46:49]
	v_mfma_f32_16x16x32_f16 v[46:49], v[74:77], v[38:41], 0
	v_mfma_f32_16x16x32_f16 v[38:41], v[98:101], v[38:41], 0
	v_mfma_f32_16x16x32_f16 v[110:113], v[106:109], v[42:45], v[38:41]
	v_mfma_f32_16x16x32_f16 v[38:41], v[74:77], v[30:33], 0
	v_mfma_f32_16x16x32_f16 v[30:33], v[98:101], v[30:33], 0
	v_mfma_f32_16x16x32_f16 v[174:177], v[106:109], v[34:37], v[30:33]
	v_mfma_f32_16x16x32_f16 v[30:33], v[74:77], v[22:25], 0
	v_mfma_f32_16x16x32_f16 v[22:25], v[98:101], v[22:25], 0
	v_mfma_f32_16x16x32_f16 v[102:105], v[86:89], v[42:45], v[46:49]
	v_mfma_f32_16x16x32_f16 v[170:173], v[86:89], v[34:37], v[38:41]
	v_mfma_f32_16x16x32_f16 v[178:181], v[86:89], v[26:29], v[30:33]
	v_mfma_f32_16x16x32_f16 v[182:185], v[106:109], v[26:29], v[22:25]
	s_setprio 0
	s_mov_b32 m0, s58
	s_barrier
	ds_read_b128 v[34:37], v237 offset:16384
	ds_read_b128 v[46:49], v237 offset:17408
	ds_read_b128 v[114:117], v237 offset:18432
	ds_read_b128 v[118:121], v237 offset:19456
	ds_read_b128 v[122:125], v237 offset:20480
	ds_read_b128 v[126:129], v237 offset:21504
	ds_read_b128 v[166:169], v237 offset:22528
	ds_read_b128 v[186:189], v237 offset:23552
	global_load_lds_dwordx4 v220, s[50:51]
	s_mov_b32 m0, s62
	s_nop 0
	global_load_lds_dwordx4 v226, s[50:51]
	s_barrier
	s_waitcnt lgkmcnt(0)
	s_setprio 1
	s_waitcnt lgkmcnt(0)
	v_mfma_f32_16x16x32_f16 v[22:25], v[6:9], v[34:37], 0
	v_mfma_f32_16x16x32_f16 v[30:33], v[6:9], v[114:117], 0
	v_mfma_f32_16x16x32_f16 v[42:45], v[6:9], v[122:125], 0
	v_mfma_f32_16x16x32_f16 v[6:9], v[6:9], v[166:169], 0
	v_mfma_f32_16x16x32_f16 v[22:25], v[10:13], v[46:49], v[22:25]
	v_mfma_f32_16x16x32_f16 v[26:29], v[14:17], v[34:37], 0
	v_mfma_f32_16x16x32_f16 v[30:33], v[10:13], v[118:121], v[30:33]
	v_mfma_f32_16x16x32_f16 v[38:41], v[14:17], v[114:117], 0
	v_mfma_f32_16x16x32_f16 v[42:45], v[10:13], v[126:129], v[42:45]
	v_mfma_f32_16x16x32_f16 v[134:137], v[14:17], v[122:125], 0
	v_mfma_f32_16x16x32_f16 v[6:9], v[10:13], v[186:189], v[6:9]
	v_mfma_f32_16x16x32_f16 v[10:13], v[14:17], v[166:169], 0
	v_mfma_f32_16x16x32_f16 v[26:29], v[18:21], v[46:49], v[26:29]
	v_mfma_f32_16x16x32_f16 v[38:41], v[18:21], v[118:121], v[38:41]
	v_mfma_f32_16x16x32_f16 v[134:137], v[18:21], v[126:129], v[134:137]
	v_mfma_f32_16x16x32_f16 v[14:17], v[18:21], v[186:189], v[10:13]
	s_setprio 0
	s_barrier
	s_add_u32 s86, s48, 0x40000
	s_addc_u32 s87, s49, 0
	s_add_i32 s84, s76, s57
	v_lshl_add_u64 v[10:11], s[86:87], 0, v[216:217]
	s_mov_b32 m0, s84
	s_add_i32 s85, s84, 0x2000
	global_load_lds_dwordx4 v[10:11], off
	v_lshl_add_u64 v[10:11], s[86:87], 0, v[218:219]
	s_mov_b32 m0, s85
	s_nop 0
	global_load_lds_dwordx4 v[10:11], off
	s_waitcnt vmcnt(6)
	s_cmp_gt_i32 s61, 44
	s_cbranch_scc1 .Lhka_done_a0
	s_cmp_lt_i32 s61, 1
	s_cbranch_scc1 .Lhka_ld_a0
	s_add_i32 s94, s61, -1
	s_lshl_b32 s94, s94, 8
	s_add_i32 s94, s94, s100
	s_mov_b32 s95, 0
	s_cmpk_gt_u32 s94, 0x15ff
	s_cselect_b32 s97, 0x7fffea00, 0
	s_cselect_b32 s96, 0x80, 0
	s_add_i32 s97, s97, s94
	s_lshl_b32 s94, s97, 1
	s_add_i32 s97, s94, 0x2c00
	s_mul_hi_u32 s98, s97, 0xba2e8ba3
	s_lshr_b32 s98, s98, 11
	s_mul_i32 s99, s98, 0x7ffff500
	s_add_i32 s99, s99, s97
	s_lshr_b32 s97, s99, 7
	s_mul_i32 s98, s98, 22
	s_add_i32 s97, s97, s98
	s_lshl_b32 s97, s97, 8
	s_and_b32 s94, s94, 0x7e
	s_or_b32 s96, s97, s96
	s_or_b32 s94, s96, s94
	s_lshl_b64 s[96:97], s[94:95], 11
	v_cvt_pk_f16_f32 v2, v2, v3
	v_cvt_pk_f16_f32 v3, v4, v5
	v_lshl_add_u64 v[4:5], v[224:225], 0, s[96:97]
	global_store_dwordx2 v[4:5], v[2:3], off
.Lhka_ld_a0:
	s_cmp_eq_u32 s61, 44
	s_cbranch_scc1 .Lhka_inc_a0
	s_lshl_b32 s94, s61, 8
	s_add_i32 s94, s94, s100
	s_mov_b32 s95, 0
	s_cmpk_gt_u32 s94, 0x15ff
	s_cselect_b64 s[96:97], -1, 0
	s_and_b64 s[96:97], s[96:97], exec
	s_cselect_b32 s96, 0x7fffea00, 0
	s_cselect_b32 s98, s25, s15
	s_cselect_b32 s99, s24, s14
	s_add_i32 s96, s96, s94
	s_lshl_b32 s94, s96, 1
	s_addk_i32 s94, 0x2c00
	s_lshl_b64 s[96:97], s[94:95], 12
	s_add_u32 s96, s99, s96
	s_addc_u32 s97, s98, s97
	v_lshlrev_b32_e32 v4, 2, v214
	v_mov_b32_e32 v5, v221
	v_lshl_add_u64 v[4:5], s[96:97], 0, v[4:5]
	global_load_dwordx4 v[2:5], v[4:5], off nt

.LBB4_30:
	v_mov_b32_e32 v227, v221
	v_lshl_add_u64 v[54:55], s[50:51], 0, v[220:221]
	v_lshl_add_u64 v[56:57], s[50:51], 0, v[226:227]
	s_add_i32 s50, 0, 0x1c000
	s_mov_b32 m0, s67
	v_add_u32_e32 v238, s50, v234
	v_lshl_add_u64 v[58:59], v[130:131], 0, s[30:31]
	ds_read_b128 v[240:243], v238
	ds_read_b128 v[244:247], v238 offset:1024
	ds_read_b128 v[248:251], v238 offset:2048
	ds_read_b128 v[252:255], v238 offset:3072
	global_load_lds_dwordx4 v[58:59], off
	v_lshl_add_u64 v[58:59], v[132:133], 0, s[30:31]
	s_mov_b32 m0, s68
	s_nop 0
	global_load_lds_dwordx4 v[58:59], off
	s_barrier
	s_waitcnt lgkmcnt(0)
	s_setprio 1
	s_waitcnt lgkmcnt(0)
	v_mfma_f32_16x16x32_f16 v[58:61], v[240:243], v[122:125], v[94:97]
	v_mfma_f32_16x16x32_f16 v[50:53], v[248:251], v[122:125], v[50:53]
	v_mfma_f32_16x16x32_f16 v[130:133], v[244:247], v[126:129], v[58:61]
	v_mfma_f32_16x16x32_f16 v[126:129], v[252:255], v[126:129], v[50:53]
	v_mfma_f32_16x16x32_f16 v[50:53], v[240:243], v[118:121], v[102:105]
	v_mfma_f32_16x16x32_f16 v[122:125], v[244:247], v[210:213], v[50:53]
	v_mfma_f32_16x16x32_f16 v[50:53], v[248:251], v[118:121], v[110:113]
	v_mfma_f32_16x16x32_f16 v[118:121], v[252:255], v[210:213], v[50:53]
	v_mfma_f32_16x16x32_f16 v[50:53], v[240:243], v[202:205], v[170:173]
	v_mfma_f32_16x16x32_f16 v[110:113], v[244:247], v[206:209], v[50:53]
	v_mfma_f32_16x16x32_f16 v[50:53], v[248:251], v[202:205], v[174:177]
	v_mfma_f32_16x16x32_f16 v[102:105], v[252:255], v[206:209], v[50:53]
	v_mfma_f32_16x16x32_f16 v[50:53], v[240:243], v[18:21], v[178:181]
	v_mfma_f32_16x16x32_f16 v[18:21], v[248:251], v[18:21], v[182:185]
	v_mfma_f32_16x16x32_f16 v[94:97], v[244:247], v[198:201], v[50:53]
	v_mfma_f32_16x16x32_f16 v[82:85], v[252:255], v[198:201], v[18:21]
	s_setprio 0
	s_mov_b32 m0, s69
	s_nop 3
	v_lshl_add_u64 v[18:19], v[54:55], 0, s[30:31]
	s_barrier
	ds_read_b128 v[66:69], v237 offset:49152
	ds_read_b128 v[78:81], v237 offset:50176
	ds_read_b128 v[170:173], v237 offset:51200
	ds_read_b128 v[174:177], v237 offset:52224
	ds_read_b128 v[178:181], v237 offset:53248
	ds_read_b128 v[182:185], v237 offset:54272
	ds_read_b128 v[198:201], v237 offset:55296
	ds_read_b128 v[202:205], v237 offset:56320
	global_load_lds_dwordx4 v[18:19], off
	v_lshl_add_u64 v[18:19], v[56:57], 0, s[30:31]
	s_mov_b32 m0, s70
	s_nop 0
	global_load_lds_dwordx4 v[18:19], off
	s_barrier
	s_waitcnt lgkmcnt(0)
	s_setprio 1
	s_waitcnt lgkmcnt(0)
	v_mfma_f32_16x16x32_f16 v[18:21], v[10:13], v[66:69], v[22:25]
	v_mfma_f32_16x16x32_f16 v[70:73], v[186:189], v[78:81], v[18:21]
	v_mfma_f32_16x16x32_f16 v[18:21], v[190:193], v[66:69], v[26:29]
	v_mfma_f32_16x16x32_f16 v[58:61], v[194:197], v[78:81], v[18:21]
	v_mfma_f32_16x16x32_f16 v[18:21], v[10:13], v[170:173], v[30:33]
	v_mfma_f32_16x16x32_f16 v[50:53], v[186:189], v[174:177], v[18:21]
	v_mfma_f32_16x16x32_f16 v[18:21], v[190:193], v[170:173], v[38:41]
	v_mfma_f32_16x16x32_f16 v[38:41], v[194:197], v[174:177], v[18:21]
	v_mfma_f32_16x16x32_f16 v[18:21], v[10:13], v[178:181], v[42:45]
	v_mfma_f32_16x16x32_f16 v[6:9], v[10:13], v[198:201], v[6:9]
	v_mfma_f32_16x16x32_f16 v[26:29], v[186:189], v[182:185], v[18:21]
	v_mfma_f32_16x16x32_f16 v[18:21], v[190:193], v[178:181], v[134:137]
	v_mfma_f32_16x16x32_f16 v[10:13], v[186:189], v[202:205], v[6:9]
	v_mfma_f32_16x16x32_f16 v[6:9], v[190:193], v[198:201], v[14:17]
	v_mfma_f32_16x16x32_f16 v[18:21], v[194:197], v[182:185], v[18:21]
	v_mfma_f32_16x16x32_f16 v[6:9], v[194:197], v[202:205], v[6:9]
	s_setprio 0
	s_barrier
	s_add_u32 s48, s48, 0x40080
	s_addc_u32 s49, s49, 0
	s_add_i32 s50, s50, s57
	v_lshl_add_u64 v[14:15], s[48:49], 0, v[216:217]
	s_mov_b32 m0, s50
	s_add_i32 s51, s50, 0x2000
	global_load_lds_dwordx4 v[14:15], off
	v_lshl_add_u64 v[14:15], s[48:49], 0, v[218:219]
	s_mov_b32 m0, s51
	s_nop 0
	global_load_lds_dwordx4 v[14:15], off
	s_waitcnt vmcnt(6)
	s_cmp_gt_i32 s61, 44
	s_cbranch_scc1 .Lhka_done_a1
	s_cmp_lt_i32 s61, 1
	s_cbranch_scc1 .Lhka_ld_a1
	s_add_i32 s94, s61, -1
	s_lshl_b32 s94, s94, 8
	s_add_i32 s94, s94, s100
	s_mov_b32 s95, 0
	s_cmpk_gt_u32 s94, 0x15ff
	s_cselect_b32 s97, 0x7fffea00, 0
	s_cselect_b32 s96, 0x80, 0
	s_add_i32 s97, s97, s94
	s_lshl_b32 s94, s97, 1
	s_add_i32 s97, s94, 0x2c00
	s_mul_hi_u32 s98, s97, 0xba2e8ba3
	s_lshr_b32 s98, s98, 11
	s_mul_i32 s99, s98, 0x7ffff500
	s_add_i32 s99, s99, s97
	s_lshr_b32 s97, s99, 7
	s_mul_i32 s98, s98, 22
	s_add_i32 s97, s97, s98
	s_lshl_b32 s97, s97, 8
	s_and_b32 s94, s94, 0x7e
	s_or_b32 s96, s97, s96
	s_or_b32 s94, s96, s94
	s_lshl_b64 s[96:97], s[94:95], 11
	v_cvt_pk_f16_f32 v2, v2, v3
	v_cvt_pk_f16_f32 v3, v4, v5
	v_lshl_add_u64 v[4:5], v[224:225], 0, s[96:97]
	global_store_dwordx2 v[4:5], v[2:3], off

.LBB4_40:
	s_add_u32 s28, s46, 0x80
	s_addc_u32 s48, s47, 0
	s_and_b64 s[44:45], s[44:45], exec
	s_cselect_b32 s45, s54, s87
	s_cselect_b32 s44, s55, s86
	s_mov_b32 m0, s59
	v_lshl_add_u64 v[182:183], s[44:45], 0, v[216:217]
	ds_read_b128 v[186:189], v229
	ds_read_b128 v[190:193], v229 offset:1024
	ds_read_b128 v[194:197], v229 offset:2048
	ds_read_b128 v[198:201], v229 offset:3072
	global_load_lds_dwordx4 v[182:183], off
	v_lshl_add_u64 v[184:185], s[44:45], 0, v[218:219]
	s_mov_b32 m0, s60
	s_cselect_b32 s49, s52, s48
	global_load_lds_dwordx4 v[184:185], off
	s_barrier
	s_waitcnt lgkmcnt(0)
	s_cselect_b32 s48, s53, s28
	s_setprio 1
	s_waitcnt lgkmcnt(0)
	v_mfma_f32_16x16x32_f16 v[130:133], v[186:189], v[174:177], v[130:133]
	v_mfma_f32_16x16x32_f16 v[126:129], v[194:197], v[174:177], v[126:129]
	v_mfma_f32_16x16x32_f16 v[122:125], v[186:189], v[166:169], v[122:125]
	v_mfma_f32_16x16x32_f16 v[118:121], v[194:197], v[166:169], v[118:121]
	v_mfma_f32_16x16x32_f16 v[110:113], v[186:189], v[158:161], v[110:113]
	v_mfma_f32_16x16x32_f16 v[102:105], v[194:197], v[158:161], v[102:105]
	v_mfma_f32_16x16x32_f16 v[94:97], v[186:189], v[150:153], v[94:97]
	v_mfma_f32_16x16x32_f16 v[82:85], v[194:197], v[150:153], v[82:85]
	v_mfma_f32_16x16x32_f16 v[130:133], v[190:193], v[178:181], v[130:133]
	v_mfma_f32_16x16x32_f16 v[126:129], v[198:201], v[178:181], v[126:129]
	v_mfma_f32_16x16x32_f16 v[122:125], v[190:193], v[170:173], v[122:125]
	v_mfma_f32_16x16x32_f16 v[118:121], v[198:201], v[170:173], v[118:121]
	v_mfma_f32_16x16x32_f16 v[110:113], v[190:193], v[162:165], v[110:113]
	v_mfma_f32_16x16x32_f16 v[102:105], v[198:201], v[162:165], v[102:105]
	v_mfma_f32_16x16x32_f16 v[94:97], v[190:193], v[154:157], v[94:97]
	v_mfma_f32_16x16x32_f16 v[82:85], v[198:201], v[154:157], v[82:85]
	s_setprio 0
	s_mov_b32 m0, s58
	s_barrier
	ds_read_b128 v[150:153], v237 offset:16384
	ds_read_b128 v[154:157], v237 offset:17408
	ds_read_b128 v[158:161], v237 offset:18432
	ds_read_b128 v[162:165], v237 offset:19456
	ds_read_b128 v[166:169], v237 offset:20480
	ds_read_b128 v[170:173], v237 offset:21504
	ds_read_b128 v[174:177], v237 offset:22528
	ds_read_b128 v[178:181], v237 offset:23552
	global_load_lds_dwordx4 v220, s[48:49]
	s_mov_b32 m0, s62
	s_nop 0
	global_load_lds_dwordx4 v226, s[48:49]
	s_barrier
	s_waitcnt lgkmcnt(0)
	s_setprio 1
	s_waitcnt lgkmcnt(0)
	v_mfma_f32_16x16x32_f16 v[70:73], v[134:137], v[150:153], v[70:73]
	v_mfma_f32_16x16x32_f16 v[58:61], v[142:145], v[150:153], v[58:61]
	v_mfma_f32_16x16x32_f16 v[50:53], v[134:137], v[158:161], v[50:53]
	v_mfma_f32_16x16x32_f16 v[38:41], v[142:145], v[158:161], v[38:41]
	v_mfma_f32_16x16x32_f16 v[26:29], v[134:137], v[166:169], v[26:29]
	v_mfma_f32_16x16x32_f16 v[18:21], v[142:145], v[166:169], v[18:21]
	v_mfma_f32_16x16x32_f16 v[10:13], v[134:137], v[174:177], v[10:13]
	v_mfma_f32_16x16x32_f16 v[6:9], v[142:145], v[174:177], v[6:9]
	v_mfma_f32_16x16x32_f16 v[70:73], v[138:141], v[154:157], v[70:73]
	v_mfma_f32_16x16x32_f16 v[58:61], v[146:149], v[154:157], v[58:61]
	v_mfma_f32_16x16x32_f16 v[50:53], v[138:141], v[162:165], v[50:53]
	v_mfma_f32_16x16x32_f16 v[38:41], v[146:149], v[162:165], v[38:41]
	v_mfma_f32_16x16x32_f16 v[26:29], v[138:141], v[170:173], v[26:29]
	v_mfma_f32_16x16x32_f16 v[18:21], v[146:149], v[170:173], v[18:21]
	v_mfma_f32_16x16x32_f16 v[10:13], v[138:141], v[178:181], v[10:13]
	v_mfma_f32_16x16x32_f16 v[6:9], v[146:149], v[178:181], v[6:9]
	s_setprio 0
	s_barrier
	s_add_u32 s90, s44, 0x40000
	s_addc_u32 s91, s45, 0
	s_mov_b32 m0, s84
	v_lshl_add_u64 v[134:135], s[90:91], 0, v[216:217]
	global_load_lds_dwordx4 v[134:135], off
	v_lshl_add_u64 v[134:135], s[90:91], 0, v[218:219]
	s_mov_b32 m0, s85
	s_nop 0
	global_load_lds_dwordx4 v[134:135], off
	s_waitcnt vmcnt(6)
	s_cmp_gt_i32 s61, 44
	s_cbranch_scc1 .Lhka_done_a2
	s_cmp_lt_i32 s61, 1
	s_cbranch_scc1 .Lhka_ld_a2
	s_add_i32 s94, s61, -1
	s_lshl_b32 s94, s94, 8
	s_add_i32 s94, s94, s100
	s_mov_b32 s95, 0
	s_cmpk_gt_u32 s94, 0x15ff
	s_cselect_b32 s97, 0x7fffea00, 0
	s_cselect_b32 s96, 0x80, 0
	s_add_i32 s97, s97, s94
	s_lshl_b32 s94, s97, 1
	s_add_i32 s97, s94, 0x2c00
	s_mul_hi_u32 s98, s97, 0xba2e8ba3
	s_lshr_b32 s98, s98, 11
	s_mul_i32 s99, s98, 0x7ffff500
	s_add_i32 s99, s99, s97
	s_lshr_b32 s97, s99, 7
	s_mul_i32 s98, s98, 22
	s_add_i32 s97, s97, s98
	s_lshl_b32 s97, s97, 8
	s_and_b32 s94, s94, 0x7e
	s_or_b32 s96, s97, s96
	s_or_b32 s94, s96, s94
	s_lshl_b64 s[96:97], s[94:95], 11
	v_cvt_pk_f16_f32 v2, v2, v3
	v_cvt_pk_f16_f32 v3, v4, v5
	v_lshl_add_u64 v[4:5], v[224:225], 0, s[96:97]
	global_store_dwordx2 v[4:5], v[2:3], off

.LBB4_46:
	s_mov_b32 m0, s67
	v_lshl_add_u64 v[182:183], v[182:183], 0, s[30:31]
	ds_read_b128 v[190:193], v238
	ds_read_b128 v[194:197], v238 offset:1024
	ds_read_b128 v[198:201], v238 offset:2048
	ds_read_b128 v[202:205], v238 offset:3072
	global_load_lds_dwordx4 v[182:183], off
	v_lshl_add_u64 v[182:183], v[184:185], 0, s[30:31]
	s_mov_b32 m0, s68
	v_mov_b32_e32 v227, v221
	global_load_lds_dwordx4 v[182:183], off
	s_barrier
	s_waitcnt lgkmcnt(0)
	v_lshl_add_u64 v[186:187], s[48:49], 0, v[220:221]
	v_lshl_add_u64 v[188:189], s[48:49], 0, v[226:227]
	s_setprio 1
	s_waitcnt lgkmcnt(0)
	v_mfma_f32_16x16x32_f16 v[130:133], v[190:193], v[174:177], v[130:133]
	v_mfma_f32_16x16x32_f16 v[126:129], v[198:201], v[174:177], v[126:129]
	v_mfma_f32_16x16x32_f16 v[122:125], v[190:193], v[166:169], v[122:125]
	v_mfma_f32_16x16x32_f16 v[118:121], v[198:201], v[166:169], v[118:121]
	v_mfma_f32_16x16x32_f16 v[110:113], v[190:193], v[158:161], v[110:113]
	v_mfma_f32_16x16x32_f16 v[102:105], v[198:201], v[158:161], v[102:105]
	v_mfma_f32_16x16x32_f16 v[94:97], v[190:193], v[150:153], v[94:97]
	v_mfma_f32_16x16x32_f16 v[82:85], v[198:201], v[150:153], v[82:85]
	v_mfma_f32_16x16x32_f16 v[130:133], v[194:197], v[178:181], v[130:133]
	v_mfma_f32_16x16x32_f16 v[126:129], v[202:205], v[178:181], v[126:129]
	v_mfma_f32_16x16x32_f16 v[122:125], v[194:197], v[170:173], v[122:125]
	v_mfma_f32_16x16x32_f16 v[118:121], v[202:205], v[170:173], v[118:121]
	v_mfma_f32_16x16x32_f16 v[110:113], v[194:197], v[162:165], v[110:113]
	v_mfma_f32_16x16x32_f16 v[102:105], v[202:205], v[162:165], v[102:105]
	v_mfma_f32_16x16x32_f16 v[94:97], v[194:197], v[154:157], v[94:97]
	v_mfma_f32_16x16x32_f16 v[82:85], v[202:205], v[154:157], v[82:85]
	s_setprio 0
	s_mov_b32 m0, s69
	v_lshl_add_u64 v[182:183], v[186:187], 0, s[30:31]
	s_barrier
	ds_read_b128 v[150:153], v237 offset:49152
	ds_read_b128 v[154:157], v237 offset:50176
	ds_read_b128 v[158:161], v237 offset:51200
	ds_read_b128 v[162:165], v237 offset:52224
	ds_read_b128 v[166:169], v237 offset:53248
	ds_read_b128 v[170:173], v237 offset:54272
	ds_read_b128 v[174:177], v237 offset:55296
	ds_read_b128 v[178:181], v237 offset:56320
	global_load_lds_dwordx4 v[182:183], off
	v_lshl_add_u64 v[182:183], v[188:189], 0, s[30:31]
	s_mov_b32 m0, s70
	s_nop 0
	global_load_lds_dwordx4 v[182:183], off
	s_barrier
	s_waitcnt lgkmcnt(0)
	s_setprio 1
	s_waitcnt lgkmcnt(0)
	v_mfma_f32_16x16x32_f16 v[70:73], v[134:137], v[150:153], v[70:73]
	v_mfma_f32_16x16x32_f16 v[58:61], v[142:145], v[150:153], v[58:61]
	v_mfma_f32_16x16x32_f16 v[50:53], v[134:137], v[158:161], v[50:53]
	v_mfma_f32_16x16x32_f16 v[38:41], v[142:145], v[158:161], v[38:41]
	v_mfma_f32_16x16x32_f16 v[26:29], v[134:137], v[166:169], v[26:29]
	v_mfma_f32_16x16x32_f16 v[18:21], v[142:145], v[166:169], v[18:21]
	v_mfma_f32_16x16x32_f16 v[10:13], v[134:137], v[174:177], v[10:13]
	v_mfma_f32_16x16x32_f16 v[6:9], v[142:145], v[174:177], v[6:9]
	v_mfma_f32_16x16x32_f16 v[70:73], v[138:141], v[154:157], v[70:73]
	v_mfma_f32_16x16x32_f16 v[58:61], v[146:149], v[154:157], v[58:61]
	v_mfma_f32_16x16x32_f16 v[50:53], v[138:141], v[162:165], v[50:53]
	v_mfma_f32_16x16x32_f16 v[38:41], v[146:149], v[162:165], v[38:41]
	v_mfma_f32_16x16x32_f16 v[26:29], v[138:141], v[170:173], v[26:29]
	v_mfma_f32_16x16x32_f16 v[18:21], v[146:149], v[170:173], v[18:21]
	v_mfma_f32_16x16x32_f16 v[10:13], v[138:141], v[178:181], v[10:13]
	v_mfma_f32_16x16x32_f16 v[6:9], v[146:149], v[178:181], v[6:9]
	s_setprio 0
	s_barrier
	s_add_u32 s44, s44, 0x40080
	s_addc_u32 s45, s45, 0
	s_mov_b32 m0, s50
	v_lshl_add_u64 v[134:135], s[44:45], 0, v[216:217]
	global_load_lds_dwordx4 v[134:135], off
	v_lshl_add_u64 v[134:135], s[44:45], 0, v[218:219]
	s_mov_b32 m0, s51
	s_nop 0
	global_load_lds_dwordx4 v[134:135], off
	s_waitcnt vmcnt(6)
	s_cmp_gt_i32 s61, 44
	s_cbranch_scc1 .Lhka_done_a3
	s_cmp_lt_i32 s61, 1
	s_cbranch_scc1 .Lhka_ld_a3
	s_add_i32 s94, s61, -1
	s_lshl_b32 s94, s94, 8
	s_add_i32 s94, s94, s100
	s_mov_b32 s95, 0
	s_cmpk_gt_u32 s94, 0x15ff
	s_cselect_b32 s97, 0x7fffea00, 0
	s_cselect_b32 s96, 0x80, 0
	s_add_i32 s97, s97, s94
	s_lshl_b32 s94, s97, 1
	s_add_i32 s97, s94, 0x2c00
	s_mul_hi_u32 s98, s97, 0xba2e8ba3
	s_lshr_b32 s98, s98, 11
	s_mul_i32 s99, s98, 0x7ffff500
	s_add_i32 s99, s99, s97
	s_lshr_b32 s97, s99, 7
	s_mul_i32 s98, s98, 22
	s_add_i32 s97, s97, s98
	s_lshl_b32 s97, s97, 8
	s_and_b32 s94, s94, 0x7e
	s_or_b32 s96, s97, s96
	s_or_b32 s94, s96, s94
	s_lshl_b64 s[96:97], s[94:95], 11
	v_cvt_pk_f16_f32 v2, v2, v3
	v_cvt_pk_f16_f32 v3, v4, v5
	v_lshl_add_u64 v[4:5], v[224:225], 0, s[96:97]
	global_store_dwordx2 v[4:5], v[2:3], off

.LBB4_53:
	s_add_i32 s0, s61, -1
	s_cmp_gt_u32 s0, 43
	s_barrier
	s_cbranch_scc1 .LBB4_55
	s_lshl_b32 s0, s0, 8
	s_add_i32 s0, s0, s100
	s_cmpk_gt_u32 s0, 0x15ff
	s_cselect_b32 s3, 0x7fffea00, 0
	s_cselect_b32 s2, 0x80, 0
	s_add_i32 s3, s3, s0
	s_lshl_b32 s0, s3, 1
	s_add_i32 s3, s0, 0x2c00
	s_mul_hi_u32 s6, s3, 0xba2e8ba3
	s_lshr_b32 s6, s6, 11
	s_mul_i32 s7, s6, 0x7ffff500
	s_add_i32 s7, s7, s3
	s_lshr_b32 s3, s7, 7
	s_mul_i32 s6, s6, 22
	s_add_i32 s3, s3, s6
	s_lshl_b32 s3, s3, 8
	s_and_b32 s0, s0, 0x7e
	s_or_b32 s2, s3, s2
	s_mov_b32 s1, 0
	s_or_b32 s0, s2, s0
	s_lshl_b64 s[0:1], s[0:1], 11
	s_waitcnt vmcnt(0)
	s_add_u32 s0, s4, s0
	v_cvt_pk_f16_f32 v1, v4, v5
	v_cvt_pk_f16_f32 v0, v2, v3
	s_addc_u32 s1, s5, s1
	v_lshlrev_b32_e32 v2, 1, v214
	global_store_dwordx2 v2, v[0:1], s[0:1]

.Lg1a_fin4:
	s_cmp_gt_i32 s61, 40
	s_cbranch_scc1 .Lg1a_fin1
	s_lshl_b32 s0, s61, 8
	s_add_i32 s0, s0, s100
	s_cmpk_gt_u32 s0, 0x15ff
	s_cselect_b32 s2, 0x7fffea00, 0
	s_cselect_b32 s4, s25, s15
	s_cselect_b32 s5, s24, s14
	s_cselect_b32 s6, 0x80, 0
	s_add_i32 s0, s0, s2
	s_lshl_b32 s7, s0, 1
	s_add_i32 s0, s7, 0x2c00
	s_lshl_b64 s[2:3], s[0:1], 12
	s_mul_hi_u32 s8, s0, 0xba2e8ba3
	s_add_u32 s2, s5, s2
	s_addc_u32 s3, s4, s3
	s_lshr_b32 s4, s8, 11
	v_lshl_add_u64 v[6:7], s[2:3], 0, v[0:1]
	s_mul_i32 s2, s4, 0x7ffff500
	s_add_i32 s2, s2, s0
	s_mul_i32 s4, s4, 22
	s_lshr_b32 s0, s2, 7
	s_add_i32 s0, s0, s4
	s_lshl_b32 s0, s0, 8
	s_and_b32 s5, s7, 0x7e
	s_or_b32 s0, s0, s6
	global_load_dwordx4 v[8:11], v[6:7], off nt
	s_or_b32 s96, s0, s5
	s_lshl_b32 s0, s61, 8
	s_add_i32 s0, s0, s100
	s_add_i32 s0, s0, 256
	s_cmpk_gt_u32 s0, 0x15ff
	s_cselect_b32 s2, 0x7fffea00, 0
	s_cselect_b32 s4, s25, s15
	s_cselect_b32 s5, s24, s14
	s_cselect_b32 s6, 0x80, 0
	s_add_i32 s0, s0, s2
	s_lshl_b32 s7, s0, 1
	s_add_i32 s0, s7, 0x2c00
	s_lshl_b64 s[2:3], s[0:1], 12
	s_mul_hi_u32 s8, s0, 0xba2e8ba3
	s_add_u32 s2, s5, s2
	s_addc_u32 s3, s4, s3
	s_lshr_b32 s4, s8, 11
	v_lshl_add_u64 v[6:7], s[2:3], 0, v[0:1]
	s_mul_i32 s2, s4, 0x7ffff500
	s_add_i32 s2, s2, s0
	s_mul_i32 s4, s4, 22
	s_lshr_b32 s0, s2, 7
	s_add_i32 s0, s0, s4
	s_lshl_b32 s0, s0, 8
	s_and_b32 s5, s7, 0x7e
	s_or_b32 s0, s0, s6
	global_load_dwordx4 v[12:15], v[6:7], off nt
	s_or_b32 s97, s0, s5
	s_lshl_b32 s0, s61, 8
	s_add_i32 s0, s0, s100
	s_add_i32 s0, s0, 512
	s_cmpk_gt_u32 s0, 0x15ff
	s_cselect_b32 s2, 0x7fffea00, 0
	s_cselect_b32 s4, s25, s15
	s_cselect_b32 s5, s24, s14
	s_cselect_b32 s6, 0x80, 0
	s_add_i32 s0, s0, s2
	s_lshl_b32 s7, s0, 1
	s_add_i32 s0, s7, 0x2c00
	s_lshl_b64 s[2:3], s[0:1], 12
	s_mul_hi_u32 s8, s0, 0xba2e8ba3
	s_add_u32 s2, s5, s2
	s_addc_u32 s3, s4, s3
	s_lshr_b32 s4, s8, 11
	v_lshl_add_u64 v[6:7], s[2:3], 0, v[0:1]
	s_mul_i32 s2, s4, 0x7ffff500
	s_add_i32 s2, s2, s0
	s_mul_i32 s4, s4, 22
	s_lshr_b32 s0, s2, 7
	s_add_i32 s0, s0, s4
	s_lshl_b32 s0, s0, 8
	s_and_b32 s5, s7, 0x7e
	s_or_b32 s0, s0, s6
	global_load_dwordx4 v[16:19], v[6:7], off nt
	s_or_b32 s98, s0, s5
	s_lshl_b32 s0, s61, 8
	s_add_i32 s0, s0, s100
	s_add_i32 s0, s0, 768
	s_cmpk_gt_u32 s0, 0x15ff
	s_cselect_b32 s2, 0x7fffea00, 0
	s_cselect_b32 s4, s25, s15
	s_cselect_b32 s5, s24, s14
	s_cselect_b32 s6, 0x80, 0
	s_add_i32 s0, s0, s2
	s_lshl_b32 s7, s0, 1
	s_add_i32 s0, s7, 0x2c00
	s_lshl_b64 s[2:3], s[0:1], 12
	s_mul_hi_u32 s8, s0, 0xba2e8ba3
	s_add_u32 s2, s5, s2
	s_addc_u32 s3, s4, s3
	s_lshr_b32 s4, s8, 11
	v_lshl_add_u64 v[6:7], s[2:3], 0, v[0:1]
	s_mul_i32 s2, s4, 0x7ffff500
	s_add_i32 s2, s2, s0
	s_mul_i32 s4, s4, 22
	s_lshr_b32 s0, s2, 7
	s_add_i32 s0, s0, s4
	s_lshl_b32 s0, s0, 8
	s_and_b32 s5, s7, 0x7e
	s_or_b32 s0, s0, s6
	global_load_dwordx4 v[20:23], v[6:7], off nt
	s_or_b32 s99, s0, s5
	s_waitcnt vmcnt(0)
	s_mov_b32 s0, s96
	s_lshl_b64 s[2:3], s[0:1], 11
	v_lshl_add_u64 v[6:7], v[224:225], 0, s[2:3]
	v_cvt_pk_f16_f32 v11, v10, v11
	v_cvt_pk_f16_f32 v10, v8, v9
	global_store_dwordx2 v[6:7], v[10:11], off
	s_mov_b32 s0, s97
	s_lshl_b64 s[2:3], s[0:1], 11
	v_lshl_add_u64 v[6:7], v[224:225], 0, s[2:3]
	v_cvt_pk_f16_f32 v15, v14, v15
	v_cvt_pk_f16_f32 v14, v12, v13
	global_store_dwordx2 v[6:7], v[14:15], off
	s_mov_b32 s0, s98
	s_lshl_b64 s[2:3], s[0:1], 11
	v_lshl_add_u64 v[6:7], v[224:225], 0, s[2:3]
	v_cvt_pk_f16_f32 v19, v18, v19
	v_cvt_pk_f16_f32 v18, v16, v17
	global_store_dwordx2 v[6:7], v[18:19], off
	s_mov_b32 s0, s99
	s_lshl_b64 s[2:3], s[0:1], 11
	v_lshl_add_u64 v[6:7], v[224:225], 0, s[2:3]
	v_cvt_pk_f16_f32 v23, v22, v23
	v_cvt_pk_f16_f32 v22, v20, v21
	global_store_dwordx2 v[6:7], v[22:23], off
	s_add_i32 s61, s61, 4
	s_branch .Lg1a_fin4

.LBB4_57:
	s_lshl_b32 s0, s61, 8
	s_add_i32 s0, s0, s100
	s_cmpk_gt_u32 s0, 0x15ff
	s_cselect_b32 s2, 0x7fffea00, 0
	s_cselect_b32 s4, s25, s15
	s_cselect_b32 s5, s24, s14
	s_cselect_b32 s6, 0x80, 0
	s_add_i32 s0, s0, s2
	s_lshl_b32 s7, s0, 1
	s_add_i32 s0, s7, 0x2c00
	s_lshl_b64 s[2:3], s[0:1], 12
	s_mul_hi_u32 s8, s0, 0xba2e8ba3
	s_add_u32 s2, s5, s2
	s_addc_u32 s3, s4, s3
	s_lshr_b32 s4, s8, 11
	v_lshl_add_u64 v[6:7], s[2:3], 0, v[0:1]
	s_mul_i32 s2, s4, 0x7ffff500
	s_add_i32 s2, s2, s0
	s_mul_i32 s4, s4, 22
	s_lshr_b32 s0, s2, 7
	s_add_i32 s0, s0, s4
	s_lshl_b32 s0, s0, 8
	s_and_b32 s5, s7, 0x7e
	s_or_b32 s0, s0, s6
	global_load_dwordx4 v[2:5], v[6:7], off nt
	s_or_b32 s0, s0, s5
	s_add_i32 s7, s61, 1
	s_waitcnt vmcnt(0)
	s_lshl_b64 s[2:3], s[0:1], 11
	v_lshl_add_u64 v[6:7], v[224:225], 0, s[2:3]
	s_cmp_gt_i32 s61, 42
	s_mov_b32 s61, s7
	v_cvt_pk_f16_f32 v5, v4, v5
	v_cvt_pk_f16_f32 v4, v2, v3
	global_store_dwordx2 v[6:7], v[4:5], off
	s_cbranch_scc0 .LBB4_57

	.amdhsa_kernel _Z7k_gemm1ILi0EEvPKDF16_S1_PDF16_PK15HIP_vector_typeIiLj2EEPKfS8_S2_PKt
		.amdhsa_group_segment_fixed_size 0
		.amdhsa_private_segment_fixed_size 0
		.amdhsa_kernarg_size 64
		.amdhsa_user_sgpr_count 2
		.amdhsa_user_sgpr_dispatch_ptr 0
		.amdhsa_user_sgpr_queue_ptr 0
		.amdhsa_user_sgpr_kernarg_segment_ptr 1
		.amdhsa_user_sgpr_dispatch_id 0
		.amdhsa_user_sgpr_kernarg_preload_length 0
		.amdhsa_user_sgpr_kernarg_preload_offset 0
		.amdhsa_user_sgpr_private_segment_size 0
		.amdhsa_uses_dynamic_stack 0
		.amdhsa_enable_private_segment 0
		.amdhsa_system_sgpr_workgroup_id_x 1
		.amdhsa_system_sgpr_workgroup_id_y 0
		.amdhsa_system_sgpr_workgroup_id_z 0
		.amdhsa_system_sgpr_workgroup_info 0
		.amdhsa_system_vgpr_workitem_id 0
		.amdhsa_next_free_vgpr 256
		.amdhsa_next_free_sgpr 101
		.amdhsa_accum_offset 256
		.amdhsa_reserve_vcc 1
		.amdhsa_float_round_mode_32 0
		.amdhsa_float_round_mode_16_64 0
		.amdhsa_float_denorm_mode_32 3
		.amdhsa_float_denorm_mode_16_64 3
		.amdhsa_dx10_clamp 1
		.amdhsa_ieee_mode 1
		.amdhsa_fp16_overflow 0
		.amdhsa_tg_split 0
		.amdhsa_exception_fp_ieee_invalid_op 0
		.amdhsa_exception_fp_denorm_src 0
		.amdhsa_exception_fp_ieee_div_zero 0
		.amdhsa_exception_fp_ieee_overflow 0
		.amdhsa_exception_fp_ieee_underflow 0
		.amdhsa_exception_fp_ieee_inexact 0
		.amdhsa_exception_int_div_zero 0
	.end_amdhsa_kernel

_Z7k_gemm1ILi1EEvPKDF16_S1_PDF16_PK15HIP_vector_typeIiLj2EEPKfS8_S2_PKt:
	s_mov_b32 s95, s2
	s_load_dwordx2 s[4:5], s[0:1], 0x18
	s_mul_i32 s6, s2, 20
	s_ashr_i32 s7, s6, 31
	s_lshl_b64 s[6:7], s[6:7], 3
	v_readfirstlane_b32 s52, v0
	s_waitcnt lgkmcnt(0)
	s_add_u32 s16, s4, s6
	s_addc_u32 s17, s5, s7
	s_load_dwordx8 s[4:11], s[16:17], 0x38
	s_load_dwordx4 s[12:15], s[16:17], 0x58
	s_load_dwordx2 s[20:21], s[16:17], 0x68
	s_mov_b32 s25, 0
	s_waitcnt lgkmcnt(0)
	s_cmp_lt_i32 s4, 0
	s_cselect_b64 s[16:17], -1, 0
	s_and_b64 vcc, exec, s[16:17]
	s_cbranch_vccnz .LBB5_2
	s_lshl_b32 s3, s5, 8
	s_and_b32 s24, s3, 0xff00
	s_bfe_u32 s3, s5, 0x80008
	s_lshl_b32 s79, s3, 1
	s_lshl_b32 s3, s4, 11
	s_and_b32 s78, s4, 0xff
	s_bfe_u32 s77, s4, 0x80010
	s_and_b32 s26, s3, 0x7f80000
	s_mov_b32 s27, s25
	s_branch .LBB5_3

.LBB5_18:
.LBB5_24:
	s_and_b64 s[46:47], s[38:39], exec
	s_cselect_b32 s48, s35, s43
	s_cselect_b32 s49, s34, s42
	s_cselect_b32 s50, s37, s41
	s_cselect_b32 s51, s36, s40
	s_add_u32 s24, s42, 0x100
	s_addc_u32 s80, s43, 0
	s_and_b64 s[46:47], s[44:45], exec
	s_cselect_b32 s47, s48, s80
	s_cselect_b32 s46, s49, s24
	s_add_u32 s24, s40, 0x100
	s_addc_u32 s80, s41, 0
	s_and_b64 s[44:45], s[44:45], exec
	s_cselect_b32 s45, s50, s80
	s_cselect_b32 s44, s51, s24
	s_mov_b32 m0, s55
	v_add_u32_e32 v227, s72, v232
	v_lshl_add_u64 v[130:131], s[44:45], 0, v[212:213]
	ds_read_b128 v[82:85], v227
	ds_read_b128 v[94:97], v227 offset:1024
	ds_read_b128 v[102:105], v227 offset:2048
	ds_read_b128 v[110:113], v227 offset:3072
	global_load_lds_dwordx4 v[130:131], off
	v_lshl_add_u64 v[132:133], s[44:45], 0, v[214:215]
	s_mov_b32 m0, s56
	s_nop 0
	global_load_lds_dwordx4 v[132:133], off
	s_barrier
	s_waitcnt lgkmcnt(0)
	s_setprio 1
	s_waitcnt lgkmcnt(0)
	v_mfma_f32_16x16x32_f16 v[90:93], v[82:85], v[46:49], 0
	v_mfma_f32_16x16x32_f16 v[46:49], v[102:105], v[46:49], 0
	v_mfma_f32_16x16x32_f16 v[90:93], v[94:97], v[50:53], v[90:93]
	v_mfma_f32_16x16x32_f16 v[46:49], v[110:113], v[50:53], v[46:49]
	v_mfma_f32_16x16x32_f16 v[50:53], v[82:85], v[38:41], 0
	v_mfma_f32_16x16x32_f16 v[38:41], v[102:105], v[38:41], 0
	v_mfma_f32_16x16x32_f16 v[106:109], v[110:113], v[42:45], v[38:41]
	v_mfma_f32_16x16x32_f16 v[38:41], v[82:85], v[30:33], 0
	v_mfma_f32_16x16x32_f16 v[30:33], v[102:105], v[30:33], 0
	v_mfma_f32_16x16x32_f16 v[170:173], v[110:113], v[34:37], v[30:33]
	v_mfma_f32_16x16x32_f16 v[30:33], v[82:85], v[22:25], 0
	v_mfma_f32_16x16x32_f16 v[22:25], v[102:105], v[22:25], 0
	v_mfma_f32_16x16x32_f16 v[98:101], v[94:97], v[42:45], v[50:53]
	v_mfma_f32_16x16x32_f16 v[166:169], v[94:97], v[34:37], v[38:41]
	v_mfma_f32_16x16x32_f16 v[174:177], v[94:97], v[26:29], v[30:33]
	v_mfma_f32_16x16x32_f16 v[178:181], v[110:113], v[26:29], v[22:25]
	s_setprio 0
	s_mov_b32 m0, s54
	s_barrier
	ds_read_b128 v[42:45], v235 offset:16384
	ds_read_b128 v[114:117], v235 offset:17408
	ds_read_b128 v[118:121], v235 offset:18432
	ds_read_b128 v[122:125], v235 offset:19456
	ds_read_b128 v[126:129], v235 offset:20480
	ds_read_b128 v[154:157], v235 offset:21504
	ds_read_b128 v[162:165], v235 offset:22528
	ds_read_b128 v[182:185], v235 offset:23552
	global_load_lds_dwordx4 v216, s[46:47]
	s_mov_b32 m0, s57
	s_nop 0
	global_load_lds_dwordx4 v222, s[46:47]
	s_barrier
	s_waitcnt lgkmcnt(0)
	s_setprio 1
	s_waitcnt lgkmcnt(0)
	v_mfma_f32_16x16x32_f16 v[22:25], v[6:9], v[42:45], 0
	v_mfma_f32_16x16x32_f16 v[30:33], v[6:9], v[118:121], 0
	v_mfma_f32_16x16x32_f16 v[38:41], v[6:9], v[126:129], 0
	v_mfma_f32_16x16x32_f16 v[6:9], v[6:9], v[162:165], 0
	v_mfma_f32_16x16x32_f16 v[22:25], v[10:13], v[114:117], v[22:25]
	v_mfma_f32_16x16x32_f16 v[26:29], v[14:17], v[42:45], 0
	v_mfma_f32_16x16x32_f16 v[30:33], v[10:13], v[122:125], v[30:33]
	v_mfma_f32_16x16x32_f16 v[34:37], v[14:17], v[118:121], 0
	v_mfma_f32_16x16x32_f16 v[38:41], v[10:13], v[154:157], v[38:41]
	v_mfma_f32_16x16x32_f16 v[50:53], v[14:17], v[126:129], 0
	v_mfma_f32_16x16x32_f16 v[6:9], v[10:13], v[182:185], v[6:9]
	v_mfma_f32_16x16x32_f16 v[10:13], v[14:17], v[162:165], 0
	v_mfma_f32_16x16x32_f16 v[26:29], v[18:21], v[114:117], v[26:29]
	v_mfma_f32_16x16x32_f16 v[34:37], v[18:21], v[122:125], v[34:37]
	v_mfma_f32_16x16x32_f16 v[50:53], v[18:21], v[154:157], v[50:53]
	v_mfma_f32_16x16x32_f16 v[14:17], v[18:21], v[182:185], v[10:13]
	s_setprio 0
	s_barrier
	s_add_u32 s82, s44, 0x40000
	s_addc_u32 s83, s45, 0
	s_add_i32 s80, s72, s53
	v_lshl_add_u64 v[10:11], s[82:83], 0, v[212:213]
	s_mov_b32 m0, s80
	s_add_i32 s81, s80, 0x2000
	global_load_lds_dwordx4 v[10:11], off
	v_lshl_add_u64 v[10:11], s[82:83], 0, v[214:215]
	s_mov_b32 m0, s81
	s_nop 0
	global_load_lds_dwordx4 v[10:11], off
	s_waitcnt vmcnt(6)
	s_cmp_gt_i32 s63, 44
	s_cbranch_scc1 .Lhkb_done_b0
	s_cmp_lt_i32 s63, 1
	s_cbranch_scc1 .Lhkb_ld_b0
	s_add_i32 s92, s63, -1
	s_lshl_b32 s92, s92, 8
	s_add_i32 s92, s92, s95
	s_mov_b32 s93, 0
	s_lshl_b64 s[90:91], s[92:93], 12
	v_cvt_pk_f16_f32 v2, v2, v3
	v_cvt_pk_f16_f32 v3, v4, v5
	v_lshl_add_u64 v[4:5], v[220:221], 0, s[90:91]
	global_store_dwordx2 v[4:5], v[2:3], off
.Lhkb_ld_b0:
	s_cmp_eq_u32 s63, 44
	s_cbranch_scc1 .Lhkb_inc_b0
	s_lshl_b32 s92, s63, 8
	s_add_i32 s92, s92, s95
	s_mov_b32 s93, 0
	s_lshl_b64 s[90:91], s[92:93], 13
	v_lshl_add_u64 v[4:5], v[224:225], 0, s[90:91]
	global_load_dwordx4 v[2:5], v[4:5], off nt

.LBB5_30:
	v_mov_b32_e32 v223, v217
	v_lshl_add_u64 v[58:59], s[46:47], 0, v[216:217]
	v_lshl_add_u64 v[60:61], s[46:47], 0, v[222:223]
	s_add_i32 s46, 0, 0x1c000
	s_mov_b32 m0, s62
	v_add_u32_e32 v236, s46, v232
	v_lshl_add_u64 v[62:63], v[130:131], 0, s[26:27]
	ds_read_b128 v[238:241], v236
	ds_read_b128 v[242:245], v236 offset:1024
	ds_read_b128 v[246:249], v236 offset:2048
	ds_read_b128 v[250:253], v236 offset:3072
	global_load_lds_dwordx4 v[62:63], off
	v_lshl_add_u64 v[62:63], v[132:133], 0, s[26:27]
	s_mov_b32 m0, s64
	s_nop 0
	global_load_lds_dwordx4 v[62:63], off
	s_barrier
	s_waitcnt lgkmcnt(0)
	s_setprio 1
	s_waitcnt lgkmcnt(0)
	v_mfma_f32_16x16x32_f16 v[62:65], v[238:241], v[122:125], v[90:93]
	v_mfma_f32_16x16x32_f16 v[46:49], v[246:249], v[122:125], v[46:49]
	v_mfma_f32_16x16x32_f16 v[130:133], v[242:245], v[126:129], v[62:65]
	v_mfma_f32_16x16x32_f16 v[126:129], v[250:253], v[126:129], v[46:49]
	v_mfma_f32_16x16x32_f16 v[46:49], v[238:241], v[114:117], v[98:101]
	v_mfma_f32_16x16x32_f16 v[122:125], v[242:245], v[206:209], v[46:49]
	v_mfma_f32_16x16x32_f16 v[46:49], v[246:249], v[114:117], v[106:109]
	v_mfma_f32_16x16x32_f16 v[114:117], v[250:253], v[206:209], v[46:49]
	v_mfma_f32_16x16x32_f16 v[46:49], v[238:241], v[198:201], v[166:169]
	v_mfma_f32_16x16x32_f16 v[106:109], v[242:245], v[202:205], v[46:49]
	v_mfma_f32_16x16x32_f16 v[46:49], v[246:249], v[198:201], v[170:173]
	v_mfma_f32_16x16x32_f16 v[98:101], v[250:253], v[202:205], v[46:49]
	v_mfma_f32_16x16x32_f16 v[46:49], v[238:241], v[18:21], v[174:177]
	v_mfma_f32_16x16x32_f16 v[18:21], v[246:249], v[18:21], v[178:181]
	v_mfma_f32_16x16x32_f16 v[90:93], v[242:245], v[194:197], v[46:49]
	v_mfma_f32_16x16x32_f16 v[78:81], v[250:253], v[194:197], v[18:21]
	s_setprio 0
	s_mov_b32 m0, s65
	s_nop 3
	v_lshl_add_u64 v[18:19], v[58:59], 0, s[26:27]
	s_barrier
	ds_read_b128 v[62:65], v235 offset:49152
	ds_read_b128 v[74:77], v235 offset:50176
	ds_read_b128 v[166:169], v235 offset:51200
	ds_read_b128 v[170:173], v235 offset:52224
	ds_read_b128 v[174:177], v235 offset:53248
	ds_read_b128 v[178:181], v235 offset:54272
	ds_read_b128 v[194:197], v235 offset:55296
	ds_read_b128 v[198:201], v235 offset:56320
	global_load_lds_dwordx4 v[18:19], off
	v_lshl_add_u64 v[18:19], v[60:61], 0, s[26:27]
	s_mov_b32 m0, s66
	s_nop 0
	global_load_lds_dwordx4 v[18:19], off
	s_barrier
	s_waitcnt lgkmcnt(0)
	s_setprio 1
	s_waitcnt lgkmcnt(0)
	v_mfma_f32_16x16x32_f16 v[18:21], v[10:13], v[62:65], v[22:25]
	v_mfma_f32_16x16x32_f16 v[70:73], v[182:185], v[74:77], v[18:21]
	v_mfma_f32_16x16x32_f16 v[18:21], v[186:189], v[62:65], v[26:29]
	v_mfma_f32_16x16x32_f16 v[58:61], v[190:193], v[74:77], v[18:21]
	v_mfma_f32_16x16x32_f16 v[18:21], v[10:13], v[166:169], v[30:33]
	v_mfma_f32_16x16x32_f16 v[46:49], v[182:185], v[170:173], v[18:21]
	v_mfma_f32_16x16x32_f16 v[18:21], v[186:189], v[166:169], v[34:37]
	v_mfma_f32_16x16x32_f16 v[34:37], v[190:193], v[170:173], v[18:21]
	v_mfma_f32_16x16x32_f16 v[18:21], v[10:13], v[174:177], v[38:41]
	v_mfma_f32_16x16x32_f16 v[6:9], v[10:13], v[194:197], v[6:9]
	v_mfma_f32_16x16x32_f16 v[26:29], v[182:185], v[178:181], v[18:21]
	v_mfma_f32_16x16x32_f16 v[18:21], v[186:189], v[174:177], v[50:53]
	v_mfma_f32_16x16x32_f16 v[10:13], v[182:185], v[198:201], v[6:9]
	v_mfma_f32_16x16x32_f16 v[6:9], v[186:189], v[194:197], v[14:17]
	v_mfma_f32_16x16x32_f16 v[18:21], v[190:193], v[178:181], v[18:21]
	v_mfma_f32_16x16x32_f16 v[6:9], v[190:193], v[198:201], v[6:9]
	s_setprio 0
	s_barrier
	s_add_u32 s44, s44, 0x40080
	s_addc_u32 s45, s45, 0
	s_add_i32 s46, s46, s53
	v_lshl_add_u64 v[14:15], s[44:45], 0, v[212:213]
	s_mov_b32 m0, s46
	s_add_i32 s47, s46, 0x2000
	global_load_lds_dwordx4 v[14:15], off
	v_lshl_add_u64 v[14:15], s[44:45], 0, v[214:215]
	s_mov_b32 m0, s47
	s_nop 0
	global_load_lds_dwordx4 v[14:15], off
	s_waitcnt vmcnt(6)
	s_cmp_gt_i32 s63, 44
	s_cbranch_scc1 .Lhkb_done_b1
	s_cmp_lt_i32 s63, 1
	s_cbranch_scc1 .Lhkb_ld_b1
	s_add_i32 s92, s63, -1
	s_lshl_b32 s92, s92, 8
	s_add_i32 s92, s92, s95
	s_mov_b32 s93, 0
	s_lshl_b64 s[90:91], s[92:93], 12
	v_cvt_pk_f16_f32 v2, v2, v3
	v_cvt_pk_f16_f32 v3, v4, v5
	v_lshl_add_u64 v[4:5], v[220:221], 0, s[90:91]
	global_store_dwordx2 v[4:5], v[2:3], off

.LBB5_40:
	s_add_u32 s24, s42, 0x80
	s_addc_u32 s44, s43, 0
	s_and_b64 s[40:41], s[40:41], exec
	s_cselect_b32 s41, s50, s83
	s_cselect_b32 s40, s51, s82
	s_mov_b32 m0, s55
	v_lshl_add_u64 v[182:183], s[40:41], 0, v[212:213]
	ds_read_b128 v[186:189], v227
	ds_read_b128 v[190:193], v227 offset:1024
	ds_read_b128 v[194:197], v227 offset:2048
	ds_read_b128 v[198:201], v227 offset:3072
	global_load_lds_dwordx4 v[182:183], off
	v_lshl_add_u64 v[184:185], s[40:41], 0, v[214:215]
	s_mov_b32 m0, s56
	s_cselect_b32 s45, s48, s44
	global_load_lds_dwordx4 v[184:185], off
	s_barrier
	s_waitcnt lgkmcnt(0)
	s_cselect_b32 s44, s49, s24
	s_setprio 1
	s_waitcnt lgkmcnt(0)
	v_mfma_f32_16x16x32_f16 v[130:133], v[186:189], v[174:177], v[130:133]
	v_mfma_f32_16x16x32_f16 v[126:129], v[194:197], v[174:177], v[126:129]
	v_mfma_f32_16x16x32_f16 v[122:125], v[186:189], v[166:169], v[122:125]
	v_mfma_f32_16x16x32_f16 v[114:117], v[194:197], v[166:169], v[114:117]
	v_mfma_f32_16x16x32_f16 v[106:109], v[186:189], v[158:161], v[106:109]
	v_mfma_f32_16x16x32_f16 v[98:101], v[194:197], v[158:161], v[98:101]
	v_mfma_f32_16x16x32_f16 v[90:93], v[186:189], v[150:153], v[90:93]
	v_mfma_f32_16x16x32_f16 v[78:81], v[194:197], v[150:153], v[78:81]
	v_mfma_f32_16x16x32_f16 v[130:133], v[190:193], v[178:181], v[130:133]
	v_mfma_f32_16x16x32_f16 v[126:129], v[198:201], v[178:181], v[126:129]
	v_mfma_f32_16x16x32_f16 v[122:125], v[190:193], v[170:173], v[122:125]
	v_mfma_f32_16x16x32_f16 v[114:117], v[198:201], v[170:173], v[114:117]
	v_mfma_f32_16x16x32_f16 v[106:109], v[190:193], v[162:165], v[106:109]
	v_mfma_f32_16x16x32_f16 v[98:101], v[198:201], v[162:165], v[98:101]
	v_mfma_f32_16x16x32_f16 v[90:93], v[190:193], v[154:157], v[90:93]
	v_mfma_f32_16x16x32_f16 v[78:81], v[198:201], v[154:157], v[78:81]
	s_setprio 0
	s_mov_b32 m0, s54
	s_barrier
	ds_read_b128 v[150:153], v235 offset:16384
	ds_read_b128 v[154:157], v235 offset:17408
	ds_read_b128 v[158:161], v235 offset:18432
	ds_read_b128 v[162:165], v235 offset:19456
	ds_read_b128 v[166:169], v235 offset:20480
	ds_read_b128 v[170:173], v235 offset:21504
	ds_read_b128 v[174:177], v235 offset:22528
	ds_read_b128 v[178:181], v235 offset:23552
	global_load_lds_dwordx4 v216, s[44:45]
	s_mov_b32 m0, s57
	s_nop 0
	global_load_lds_dwordx4 v222, s[44:45]
	s_barrier
	s_waitcnt lgkmcnt(0)
	s_setprio 1
	s_waitcnt lgkmcnt(0)
	v_mfma_f32_16x16x32_f16 v[70:73], v[134:137], v[150:153], v[70:73]
	v_mfma_f32_16x16x32_f16 v[58:61], v[142:145], v[150:153], v[58:61]
	v_mfma_f32_16x16x32_f16 v[46:49], v[134:137], v[158:161], v[46:49]
	v_mfma_f32_16x16x32_f16 v[34:37], v[142:145], v[158:161], v[34:37]
	v_mfma_f32_16x16x32_f16 v[26:29], v[134:137], v[166:169], v[26:29]
	v_mfma_f32_16x16x32_f16 v[18:21], v[142:145], v[166:169], v[18:21]
	v_mfma_f32_16x16x32_f16 v[10:13], v[134:137], v[174:177], v[10:13]
	v_mfma_f32_16x16x32_f16 v[6:9], v[142:145], v[174:177], v[6:9]
	v_mfma_f32_16x16x32_f16 v[70:73], v[138:141], v[154:157], v[70:73]
	v_mfma_f32_16x16x32_f16 v[58:61], v[146:149], v[154:157], v[58:61]
	v_mfma_f32_16x16x32_f16 v[46:49], v[138:141], v[162:165], v[46:49]
	v_mfma_f32_16x16x32_f16 v[34:37], v[146:149], v[162:165], v[34:37]
	v_mfma_f32_16x16x32_f16 v[26:29], v[138:141], v[170:173], v[26:29]
	v_mfma_f32_16x16x32_f16 v[18:21], v[146:149], v[170:173], v[18:21]
	v_mfma_f32_16x16x32_f16 v[10:13], v[138:141], v[178:181], v[10:13]
	v_mfma_f32_16x16x32_f16 v[6:9], v[146:149], v[178:181], v[6:9]
	s_setprio 0
	s_barrier
	s_add_u32 s86, s40, 0x40000
	s_addc_u32 s87, s41, 0
	s_mov_b32 m0, s80
	v_lshl_add_u64 v[134:135], s[86:87], 0, v[212:213]
	global_load_lds_dwordx4 v[134:135], off
	v_lshl_add_u64 v[134:135], s[86:87], 0, v[214:215]
	s_mov_b32 m0, s81
	s_nop 0
	global_load_lds_dwordx4 v[134:135], off
	s_waitcnt vmcnt(6)
	s_cmp_gt_i32 s63, 44
	s_cbranch_scc1 .Lhkb_done_b2
	s_cmp_lt_i32 s63, 1
	s_cbranch_scc1 .Lhkb_ld_b2
	s_add_i32 s92, s63, -1
	s_lshl_b32 s92, s92, 8
	s_add_i32 s92, s92, s95
	s_mov_b32 s93, 0
	s_lshl_b64 s[90:91], s[92:93], 12
	v_cvt_pk_f16_f32 v2, v2, v3
	v_cvt_pk_f16_f32 v3, v4, v5
	v_lshl_add_u64 v[4:5], v[220:221], 0, s[90:91]
	global_store_dwordx2 v[4:5], v[2:3], off

.LBB5_46:
	s_mov_b32 m0, s62
	v_lshl_add_u64 v[182:183], v[182:183], 0, s[26:27]
	ds_read_b128 v[190:193], v236
	ds_read_b128 v[194:197], v236 offset:1024
	ds_read_b128 v[198:201], v236 offset:2048
	ds_read_b128 v[202:205], v236 offset:3072
	global_load_lds_dwordx4 v[182:183], off
	v_lshl_add_u64 v[182:183], v[184:185], 0, s[26:27]
	s_mov_b32 m0, s64
	v_mov_b32_e32 v223, v217
	global_load_lds_dwordx4 v[182:183], off
	s_barrier
	s_waitcnt lgkmcnt(0)
	v_lshl_add_u64 v[186:187], s[44:45], 0, v[216:217]
	v_lshl_add_u64 v[188:189], s[44:45], 0, v[222:223]
	s_setprio 1
	s_waitcnt lgkmcnt(0)
	v_mfma_f32_16x16x32_f16 v[130:133], v[190:193], v[174:177], v[130:133]
	v_mfma_f32_16x16x32_f16 v[126:129], v[198:201], v[174:177], v[126:129]
	v_mfma_f32_16x16x32_f16 v[122:125], v[190:193], v[166:169], v[122:125]
	v_mfma_f32_16x16x32_f16 v[114:117], v[198:201], v[166:169], v[114:117]
	v_mfma_f32_16x16x32_f16 v[106:109], v[190:193], v[158:161], v[106:109]
	v_mfma_f32_16x16x32_f16 v[98:101], v[198:201], v[158:161], v[98:101]
	v_mfma_f32_16x16x32_f16 v[90:93], v[190:193], v[150:153], v[90:93]
	v_mfma_f32_16x16x32_f16 v[78:81], v[198:201], v[150:153], v[78:81]
	v_mfma_f32_16x16x32_f16 v[130:133], v[194:197], v[178:181], v[130:133]
	v_mfma_f32_16x16x32_f16 v[126:129], v[202:205], v[178:181], v[126:129]
	v_mfma_f32_16x16x32_f16 v[122:125], v[194:197], v[170:173], v[122:125]
	v_mfma_f32_16x16x32_f16 v[114:117], v[202:205], v[170:173], v[114:117]
	v_mfma_f32_16x16x32_f16 v[106:109], v[194:197], v[162:165], v[106:109]
	v_mfma_f32_16x16x32_f16 v[98:101], v[202:205], v[162:165], v[98:101]
	v_mfma_f32_16x16x32_f16 v[90:93], v[194:197], v[154:157], v[90:93]
	v_mfma_f32_16x16x32_f16 v[78:81], v[202:205], v[154:157], v[78:81]
	s_setprio 0
	s_mov_b32 m0, s65
	v_lshl_add_u64 v[182:183], v[186:187], 0, s[26:27]
	s_barrier
	ds_read_b128 v[150:153], v235 offset:49152
	ds_read_b128 v[154:157], v235 offset:50176
	ds_read_b128 v[158:161], v235 offset:51200
	ds_read_b128 v[162:165], v235 offset:52224
	ds_read_b128 v[166:169], v235 offset:53248
	ds_read_b128 v[170:173], v235 offset:54272
	ds_read_b128 v[174:177], v235 offset:55296
	ds_read_b128 v[178:181], v235 offset:56320
	global_load_lds_dwordx4 v[182:183], off
	v_lshl_add_u64 v[182:183], v[188:189], 0, s[26:27]
	s_mov_b32 m0, s66
	s_nop 0
	global_load_lds_dwordx4 v[182:183], off
	s_barrier
	s_waitcnt lgkmcnt(0)
	s_setprio 1
	s_waitcnt lgkmcnt(0)
	v_mfma_f32_16x16x32_f16 v[70:73], v[134:137], v[150:153], v[70:73]
	v_mfma_f32_16x16x32_f16 v[58:61], v[142:145], v[150:153], v[58:61]
	v_mfma_f32_16x16x32_f16 v[46:49], v[134:137], v[158:161], v[46:49]
	v_mfma_f32_16x16x32_f16 v[34:37], v[142:145], v[158:161], v[34:37]
	v_mfma_f32_16x16x32_f16 v[26:29], v[134:137], v[166:169], v[26:29]
	v_mfma_f32_16x16x32_f16 v[18:21], v[142:145], v[166:169], v[18:21]
	v_mfma_f32_16x16x32_f16 v[10:13], v[134:137], v[174:177], v[10:13]
	v_mfma_f32_16x16x32_f16 v[6:9], v[142:145], v[174:177], v[6:9]
	v_mfma_f32_16x16x32_f16 v[70:73], v[138:141], v[154:157], v[70:73]
	v_mfma_f32_16x16x32_f16 v[58:61], v[146:149], v[154:157], v[58:61]
	v_mfma_f32_16x16x32_f16 v[46:49], v[138:141], v[162:165], v[46:49]
	v_mfma_f32_16x16x32_f16 v[34:37], v[146:149], v[162:165], v[34:37]
	v_mfma_f32_16x16x32_f16 v[26:29], v[138:141], v[170:173], v[26:29]
	v_mfma_f32_16x16x32_f16 v[18:21], v[146:149], v[170:173], v[18:21]
	v_mfma_f32_16x16x32_f16 v[10:13], v[138:141], v[178:181], v[10:13]
	v_mfma_f32_16x16x32_f16 v[6:9], v[146:149], v[178:181], v[6:9]
	s_setprio 0
	s_barrier
	s_add_u32 s40, s40, 0x40080
	s_addc_u32 s41, s41, 0
	s_mov_b32 m0, s46
	v_lshl_add_u64 v[134:135], s[40:41], 0, v[212:213]
	global_load_lds_dwordx4 v[134:135], off
	v_lshl_add_u64 v[134:135], s[40:41], 0, v[214:215]
	s_mov_b32 m0, s47
	s_nop 0
	global_load_lds_dwordx4 v[134:135], off
	s_waitcnt vmcnt(6)
	s_cmp_gt_i32 s63, 44
	s_cbranch_scc1 .Lhkb_done_b3
	s_cmp_lt_i32 s63, 1
	s_cbranch_scc1 .Lhkb_ld_b3
	s_add_i32 s92, s63, -1
	s_lshl_b32 s92, s92, 8
	s_add_i32 s92, s92, s95
	s_mov_b32 s93, 0
	s_lshl_b64 s[90:91], s[92:93], 12
	v_cvt_pk_f16_f32 v2, v2, v3
	v_cvt_pk_f16_f32 v3, v4, v5
	v_lshl_add_u64 v[4:5], v[220:221], 0, s[90:91]
	global_store_dwordx2 v[4:5], v[2:3], off

.LBB5_53:
	s_add_i32 s0, s63, -1
	s_cmp_gt_u32 s0, 43
	s_barrier
	s_cbranch_scc1 .LBB5_55
	s_lshl_b32 s0, s0, 8
	s_add_i32 s0, s0, s95
	s_mov_b32 s1, 0
	s_lshl_b64 s[0:1], s[0:1], 12
	s_waitcnt vmcnt(0)
	s_add_u32 s0, s4, s0
	v_cvt_pk_f16_f32 v1, v4, v5
	v_cvt_pk_f16_f32 v0, v2, v3
	s_addc_u32 s1, s5, s1
	v_lshlrev_b32_e32 v2, 1, v210
	global_store_dwordx2 v2, v[0:1], s[0:1]

.Lg1b_fin4:
	s_cmp_gt_i32 s63, 40
	s_cbranch_scc1 .Lg1b_fin1
	s_lshl_b32 s0, s63, 8
	s_add_i32 s0, s0, s95
	s_lshl_b64 s[2:3], s[0:1], 13
	v_lshl_add_u64 v[4:5], v[224:225], 0, s[2:3]
	global_load_dwordx4 v[6:9], v[4:5], off nt
	s_add_u32 s2, s2, 0x200000
	s_addc_u32 s3, s3, 0
	v_lshl_add_u64 v[4:5], v[224:225], 0, s[2:3]
	global_load_dwordx4 v[10:13], v[4:5], off nt
	s_add_u32 s2, s2, 0x200000
	s_addc_u32 s3, s3, 0
	v_lshl_add_u64 v[4:5], v[224:225], 0, s[2:3]
	global_load_dwordx4 v[14:17], v[4:5], off nt
	s_add_u32 s2, s2, 0x200000
	s_addc_u32 s3, s3, 0
	v_lshl_add_u64 v[4:5], v[224:225], 0, s[2:3]
	global_load_dwordx4 v[18:21], v[4:5], off nt
	s_lshl_b64 s[2:3], s[0:1], 12
	s_waitcnt vmcnt(0)
	v_lshl_add_u64 v[4:5], v[220:221], 0, s[2:3]
	v_cvt_pk_f16_f32 v9, v8, v9
	v_cvt_pk_f16_f32 v8, v6, v7
	global_store_dwordx2 v[4:5], v[8:9], off
	s_add_u32 s2, s2, 0x100000
	s_addc_u32 s3, s3, 0
	v_lshl_add_u64 v[4:5], v[220:221], 0, s[2:3]
	v_cvt_pk_f16_f32 v13, v12, v13
	v_cvt_pk_f16_f32 v12, v10, v11
	global_store_dwordx2 v[4:5], v[12:13], off
	s_add_u32 s2, s2, 0x100000
	s_addc_u32 s3, s3, 0
	v_lshl_add_u64 v[4:5], v[220:221], 0, s[2:3]
	v_cvt_pk_f16_f32 v17, v16, v17
	v_cvt_pk_f16_f32 v16, v14, v15
	global_store_dwordx2 v[4:5], v[16:17], off
	s_add_u32 s2, s2, 0x100000
	s_addc_u32 s3, s3, 0
	v_lshl_add_u64 v[4:5], v[220:221], 0, s[2:3]
	v_cvt_pk_f16_f32 v21, v20, v21
	v_cvt_pk_f16_f32 v20, v18, v19
	global_store_dwordx2 v[4:5], v[20:21], off
	s_add_u32 s2, s2, 0x100000
	s_addc_u32 s3, s3, 0
	s_add_i32 s63, s63, 4
	s_branch .Lg1b_fin4

.LBB5_57:
	s_lshl_b32 s0, s63, 8
	s_add_i32 s0, s0, s95
	s_lshl_b64 s[2:3], s[0:1], 13
	v_lshl_add_u64 v[4:5], v[224:225], 0, s[2:3]
	global_load_dwordx4 v[0:3], v[4:5], off nt
	s_add_i32 s4, s63, 1
	s_lshl_b64 s[2:3], s[0:1], 12
	s_waitcnt vmcnt(0)
	v_lshl_add_u64 v[4:5], v[220:221], 0, s[2:3]
	s_cmp_gt_i32 s63, 42
	s_mov_b32 s63, s4
	v_cvt_pk_f16_f32 v3, v2, v3
	v_cvt_pk_f16_f32 v2, v0, v1
	global_store_dwordx2 v[4:5], v[2:3], off
	s_cbranch_scc0 .LBB5_57

	.amdhsa_kernel _Z7k_gemm1ILi1EEvPKDF16_S1_PDF16_PK15HIP_vector_typeIiLj2EEPKfS8_S2_PKt
		.amdhsa_group_segment_fixed_size 0
		.amdhsa_private_segment_fixed_size 0
		.amdhsa_kernarg_size 64
		.amdhsa_user_sgpr_count 2
		.amdhsa_user_sgpr_dispatch_ptr 0
		.amdhsa_user_sgpr_queue_ptr 0
		.amdhsa_user_sgpr_kernarg_segment_ptr 1
		.amdhsa_user_sgpr_dispatch_id 0
		.amdhsa_user_sgpr_kernarg_preload_length 0
		.amdhsa_user_sgpr_kernarg_preload_offset 0
		.amdhsa_user_sgpr_private_segment_size 0
		.amdhsa_uses_dynamic_stack 0
		.amdhsa_enable_private_segment 0
		.amdhsa_system_sgpr_workgroup_id_x 1
		.amdhsa_system_sgpr_workgroup_id_y 0
		.amdhsa_system_sgpr_workgroup_id_z 0
		.amdhsa_system_sgpr_workgroup_info 0
		.amdhsa_system_vgpr_workitem_id 0
		.amdhsa_next_free_vgpr 254
		.amdhsa_next_free_sgpr 96
		.amdhsa_accum_offset 256
		.amdhsa_reserve_vcc 1
		.amdhsa_float_round_mode_32 0
		.amdhsa_float_round_mode_16_64 0
		.amdhsa_float_denorm_mode_32 3
		.amdhsa_float_denorm_mode_16_64 3
		.amdhsa_dx10_clamp 1
		.amdhsa_ieee_mode 1
		.amdhsa_fp16_overflow 0
		.amdhsa_tg_split 0
		.amdhsa_exception_fp_ieee_invalid_op 0
		.amdhsa_exception_fp_denorm_src 0
		.amdhsa_exception_fp_ieee_div_zero 0
		.amdhsa_exception_fp_ieee_overflow 0
		.amdhsa_exception_fp_ieee_underflow 0
		.amdhsa_exception_fp_ieee_inexact 0
		.amdhsa_exception_int_div_zero 0
	.end_amdhsa_kernel

amdhsa.kernels:
  - .agpr_count:     0
    .args:
      - .actual_access:  read_only
        .address_space:  global
        .offset:         0
        .size:           8
        .value_kind:     global_buffer
      - .actual_access:  read_only
        .address_space:  global
        .offset:         8
        .size:           8
        .value_kind:     global_buffer
      - .actual_access:  write_only
        .address_space:  global
        .offset:         16
        .size:           8
        .value_kind:     global_buffer
      - .actual_access:  write_only
        .address_space:  global
        .offset:         24
        .size:           8
        .value_kind:     global_buffer
      - .actual_access:  write_only
        .address_space:  global
        .offset:         32
        .size:           8
        .value_kind:     global_buffer
      - .actual_access:  write_only
        .address_space:  global
        .offset:         40
        .size:           8
        .value_kind:     global_buffer
    .group_segment_fixed_size: 256
    .kernarg_segment_align: 8
    .kernarg_segment_size: 48
    .language:       OpenCL C
    .language_version:
      - 2
      - 0
    .max_flat_workgroup_size: 256
    .name:           _Z10k_xscatterPKiS0_P15HIP_vector_typeIiLj2EEPtP4MetaS3_
    .private_segment_fixed_size: 0
    .sgpr_count:     41
    .sgpr_spill_count: 0
    .symbol:         _Z10k_xscatterPKiS0_P15HIP_vector_typeIiLj2EEPtP4MetaS3_.kd
    .uniform_work_group_size: 1
    .uses_dynamic_stack: false
    .vgpr_count:     55
    .vgpr_spill_count: 0
    .wavefront_size: 64
  - .agpr_count:     0
    .args:
      - .actual_access:  read_only
        .address_space:  global
        .offset:         0
        .size:           8
        .value_kind:     global_buffer
      - .actual_access:  read_only
        .address_space:  global
        .offset:         8
        .size:           8
        .value_kind:     global_buffer
      - .actual_access:  write_only
        .address_space:  global
        .offset:         16
        .size:           8
        .value_kind:     global_buffer
      - .actual_access:  write_only
        .address_space:  global
        .offset:         24
        .size:           8
        .value_kind:     global_buffer
      - .actual_access:  write_only
        .address_space:  global
        .offset:         32
        .size:           8
        .value_kind:     global_buffer
      - .actual_access:  read_only
        .address_space:  global
        .offset:         40
        .size:           8
        .value_kind:     global_buffer
      - .actual_access:  read_only
        .address_space:  global
        .offset:         48
        .size:           8
        .value_kind:     global_buffer
      - .actual_access:  write_only
        .address_space:  global
        .offset:         56
        .size:           8
        .value_kind:     global_buffer
      - .actual_access:  write_only
        .address_space:  global
        .offset:         64
        .size:           8
        .value_kind:     global_buffer
    .group_segment_fixed_size: 4096
    .kernarg_segment_align: 8
    .kernarg_segment_size: 72
    .language:       OpenCL C
    .language_version:
      - 2
      - 0
    .max_flat_workgroup_size: 256
    .name:           _Z5k_prePKfS0_PiP15HIP_vector_typeIfLj2EES1_S0_S0_PDF16_S5_
    .private_segment_fixed_size: 0
    .sgpr_count:     42
    .sgpr_spill_count: 0
    .symbol:         _Z5k_prePKfS0_PiP15HIP_vector_typeIfLj2EES1_S0_S0_PDF16_S5_.kd
    .uniform_work_group_size: 1
    .uses_dynamic_stack: false
    .vgpr_count:     128
    .vgpr_spill_count: 0
    .wavefront_size: 64
  - .agpr_count:     0
    .args:
      - .address_space:  global
        .offset:         0
        .size:           8
        .value_kind:     global_buffer
      - .address_space:  global
        .offset:         8
        .size:           8
        .value_kind:     global_buffer
      - .actual_access:  write_only
        .address_space:  global
        .offset:         16
        .size:           8
        .value_kind:     global_buffer
      - .actual_access:  read_only
        .address_space:  global
        .offset:         24
        .size:           8
        .value_kind:     global_buffer
    .group_segment_fixed_size: 0
    .kernarg_segment_align: 8
    .kernarg_segment_size: 32
    .language:       OpenCL C
    .language_version:
      - 2
      - 0
    .max_flat_workgroup_size: 512
    .name:           _Z7k_gemm2PKDF16_S0_PDF16_PK15HIP_vector_typeIiLj2EE
    .private_segment_fixed_size: 0
    .sgpr_count:     74
    .sgpr_spill_count: 0
    .symbol:         _Z7k_gemm2PKDF16_S0_PDF16_PK15HIP_vector_typeIiLj2EE.kd
    .uniform_work_group_size: 1
    .uses_dynamic_stack: false
    .vgpr_count:     226
    .vgpr_spill_count: 0
    .wavefront_size: 64
  - .agpr_count:     0
    .args:
      - .actual_access:  read_only
        .address_space:  global
        .offset:         0
        .size:           8
        .value_kind:     global_buffer
      - .actual_access:  read_only
        .address_space:  global
        .offset:         8
        .size:           8
        .value_kind:     global_buffer
      - .actual_access:  read_only
        .address_space:  global
        .offset:         16
        .size:           8
        .value_kind:     global_buffer
      - .actual_access:  write_only
        .address_space:  global
        .offset:         24
        .size:           8
        .value_kind:     global_buffer
    .group_segment_fixed_size: 0
    .kernarg_segment_align: 8
    .kernarg_segment_size: 32
    .language:       OpenCL C
    .language_version:
      - 2
      - 0
    .max_flat_workgroup_size: 256
    .name:           _Z9k_combinePKDF16_PK15HIP_vector_typeIiLj2EEPKS1_IfLj2EEPf
    .private_segment_fixed_size: 0
    .sgpr_count:     30
    .sgpr_spill_count: 0
    .symbol:         _Z9k_combinePKDF16_PK15HIP_vector_typeIiLj2EEPKS1_IfLj2EEPf.kd
    .uniform_work_group_size: 1
    .uses_dynamic_stack: false
    .vgpr_count:     64
    .vgpr_spill_count: 0
    .wavefront_size: 64
  - .agpr_count:     0
    .args:
      - .address_space:  global
        .offset:         0
        .size:           8
        .value_kind:     global_buffer
      - .address_space:  global
        .offset:         8
        .size:           8
        .value_kind:     global_buffer
      - .actual_access:  write_only
        .address_space:  global
        .offset:         16
        .size:           8
        .value_kind:     global_buffer
      - .actual_access:  read_only
        .address_space:  global
        .offset:         24
        .size:           8
        .value_kind:     global_buffer
      - .address_space:  global
        .offset:         32
        .size:           8
        .value_kind:     global_buffer
      - .address_space:  global
        .offset:         40
        .size:           8
        .value_kind:     global_buffer
      - .actual_access:  write_only
        .address_space:  global
        .offset:         48
        .size:           8
        .value_kind:     global_buffer
      - .address_space:  global
        .offset:         56
        .size:           8
        .value_kind:     global_buffer
    .group_segment_fixed_size: 0
    .kernarg_segment_align: 8
    .kernarg_segment_size: 64
    .language:       OpenCL C
    .language_version:
      - 2
      - 0
    .max_flat_workgroup_size: 512
    .name:           _Z7k_gemm1ILi0EEvPKDF16_S1_PDF16_PK15HIP_vector_typeIiLj2EEPKfS8_S2_PKt
    .private_segment_fixed_size: 0
    .sgpr_count:     107
    .sgpr_spill_count: 0
    .symbol:         _Z7k_gemm1ILi0EEvPKDF16_S1_PDF16_PK15HIP_vector_typeIiLj2EEPKfS8_S2_PKt.kd
    .uniform_work_group_size: 1
    .uses_dynamic_stack: false
    .vgpr_count:     256
    .vgpr_spill_count: 0
    .wavefront_size: 64
  - .agpr_count:     0
    .args:
      - .address_space:  global
        .offset:         0
        .size:           8
        .value_kind:     global_buffer
      - .address_space:  global
        .offset:         8
        .size:           8
        .value_kind:     global_buffer
      - .actual_access:  write_only
        .address_space:  global
        .offset:         16
        .size:           8
        .value_kind:     global_buffer
      - .actual_access:  read_only
        .address_space:  global
        .offset:         24
        .size:           8
        .value_kind:     global_buffer
      - .address_space:  global
        .offset:         32
        .size:           8
        .value_kind:     global_buffer
      - .actual_access:  read_only
        .address_space:  global
        .offset:         40
        .size:           8
        .value_kind:     global_buffer
      - .actual_access:  write_only
        .address_space:  global
        .offset:         48
        .size:           8
        .value_kind:     global_buffer
      - .address_space:  global
        .offset:         56
        .size:           8
        .value_kind:     global_buffer
    .group_segment_fixed_size: 0
    .kernarg_segment_align: 8
    .kernarg_segment_size: 64
    .language:       OpenCL C
    .language_version:
      - 2
      - 0
    .max_flat_workgroup_size: 512
    .name:           _Z7k_gemm1ILi1EEvPKDF16_S1_PDF16_PK15HIP_vector_typeIiLj2EEPKfS8_S2_PKt
    .private_segment_fixed_size: 0
    .sgpr_count:     102
    .sgpr_spill_count: 0
    .symbol:         _Z7k_gemm1ILi1EEvPKDF16_S1_PDF16_PK15HIP_vector_typeIiLj2EEPKfS8_S2_PKt.kd
    .uniform_work_group_size: 1
    .uses_dynamic_stack: false
    .vgpr_count:     254
    .vgpr_spill_count: 0
    .wavefront_size: 64
